# nca1: logical wave roles swapped (tid ^= 256 at entry) so the older hardware waves 0-3 take the long-tail hh=1 role (heads/sigmoid) and win VALU arbitration
# speedup vs baseline: 1.0097x; 1.0097x over previous
_Z5k_ncaILi1EEvPKDF16_S1_PKfS3_PDF16_S3_S3_S3_S3_Pf:
	v_xor_b32_e32 v0, 0x100, v0
	s_lshl_b32 s3, s2, 1
	s_and_b32 s3, s3, 12
	s_lshr_b32 s4, s2, 6
	s_add_i32 s3, s3, s4
	v_lshrrev_b32_e32 v1, 5, v0
	s_lshl_b32 s4, s2, 6
	v_and_b32_e32 v76, 4, v1
	s_lshl_b32 s29, s3, 3
	s_load_dwordx4 s[20:23], s[0:1], 0x0
	s_and_b32 s4, s4, 64
	s_and_b32 s2, s2, 56
	v_bfe_u32 v60, v0, 2, 2
	v_or_b32_e32 v58, s29, v76
	s_or_b32 s28, s4, s2
	v_lshrrev_b32_e32 v52, 4, v0
	v_or_b32_e32 v2, v58, v60
	v_and_b32_e32 v57, 4, v52
	v_and_b32_e32 v1, 3, v0
	v_lshl_or_b32 v2, v2, 7, s28
	v_or3_b32 v56, v2, v57, v1
	s_movk_i32 s4, 0x48
	v_mul_lo_u32 v2, v56, s4
	v_mov_b32_e32 v3, 0
	s_waitcnt lgkmcnt(0)
	v_lshl_add_u64 v[6:7], v[2:3], 1, s[20:21]
	v_and_b32_e32 v2, 48, v0
	v_lshl_add_u64 v[8:9], v[6:7], 0, v[2:3]
	global_load_dwordx4 v[2:5], v[8:9], off offset:64
	global_load_dwordx4 v[10:13], v[8:9], off
	global_load_dwordx4 v[22:25], v[6:7], off offset:128
	v_mul_u32_u24_e32 v6, 0x1c72, v0
	v_mul_u32_u24_e32 v78, 0x195, v0
	s_movk_i32 s2, 0xffee
	s_add_i32 s29, s29, -5
	s_add_i32 s30, s28, -5
	v_lshrrev_b32_e32 v77, 16, v6
	v_mul_i32_i24_sdwa v6, v78, s2 dst_sel:DWORD dst_unused:UNUSED_PAD src0_sel:WORD_1 src1_sel:DWORD
	v_add_u32_sdwa v14, s29, v78 dst_sel:DWORD dst_unused:UNUSED_PAD src0_sel:DWORD src1_sel:WORD_1
	v_add3_u32 v15, s30, v77, v6
	v_or_b32_e32 v6, v15, v14
	s_movk_i32 s5, 0x80
	v_cmp_gt_u32_e32 vcc, s5, v6
	v_mov_b64_e32 v[6:7], 0
	v_mov_b64_e32 v[8:9], 0
	s_and_saveexec_b64 s[2:3], vcc
	v_lshl_or_b32 v9, v14, 7, v15
	v_mad_i32_i24 v8, v77, -9, v0
	v_mul_lo_u32 v9, v9, s4
	v_lshl_add_u32 v8, v8, 3, v9
	v_ashrrev_i32_e32 v9, 31, v8
	s_or_b64 exec, exec, s[2:3]
	v_lshl_add_u64 v[8:9], v[8:9], 1, s[22:23]
	global_load_dwordx4 v[26:29], v[8:9], off
	v_or_b32_e32 v62, 0x200, v0
	v_mul_u32_u24_e32 v8, 0x1c72, v62
	v_lshrrev_b32_e32 v79, 16, v8
	v_mul_u32_u24_e32 v8, 0x653, v62
	v_lshrrev_b32_e32 v80, 18, v8
	v_mul_i32_i24_e32 v9, 0xffffffee, v80
	v_add_u32_e32 v8, s29, v80
	v_add3_u32 v9, s30, v79, v9
	v_or_b32_e32 v14, v9, v8
	v_cmp_gt_u32_e64 s[2:3], s5, v14
	s_and_saveexec_b64 s[4:5], s[2:3]
	v_lshl_or_b32 v7, v8, 7, v9
	s_movk_i32 s6, 0x48
	v_mad_i32_i24 v6, v79, -9, v62
	v_mul_lo_u32 v7, v7, s6
	v_lshl_add_u32 v6, v6, 3, v7
	v_ashrrev_i32_e32 v7, 31, v6
	s_or_b64 exec, exec, s[4:5]
	v_lshl_add_u64 v[6:7], v[6:7], 1, s[22:23]
	global_load_dwordx4 v[30:33], v[6:7], off
	v_or_b32_e32 v61, 0x400, v0
	v_mul_u32_u24_e32 v6, 0x1c72, v61
	v_lshrrev_b32_e32 v81, 16, v6
	v_mul_u32_u24_e32 v6, 0x653, v61
	v_lshrrev_b32_e32 v82, 18, v6
	v_mul_i32_i24_e32 v6, 0xffffffee, v82
	v_add_u32_e32 v14, s29, v82
	v_add3_u32 v15, s30, v81, v6
	v_or_b32_e32 v6, v15, v14
	s_movk_i32 s8, 0x80
	v_cmp_gt_u32_e64 s[4:5], s8, v6
	v_mov_b64_e32 v[6:7], 0
	v_mov_b64_e32 v[8:9], 0
	s_and_saveexec_b64 s[6:7], s[4:5]
	v_lshl_or_b32 v9, v14, 7, v15
	s_movk_i32 s9, 0x48
	v_mad_i32_i24 v8, v81, -9, v61
	v_mul_lo_u32 v9, v9, s9
	v_lshl_add_u32 v8, v8, 3, v9
	v_mov_b32_e32 v9, 0
	s_or_b64 exec, exec, s[6:7]
	v_lshl_add_u64 v[8:9], v[8:9], 1, s[22:23]
	global_load_dwordx4 v[34:37], v[8:9], off
	v_or_b32_e32 v83, 0x600, v0
	v_mul_u32_u24_e32 v8, 0x1c72, v83
	v_lshrrev_b32_e32 v84, 16, v8
	v_mul_u32_u24_e32 v8, 0x653, v83
	v_lshrrev_b32_e32 v85, 18, v8
	v_mul_i32_i24_e32 v9, 0xffffffee, v85
	v_add_u32_e32 v8, s29, v85
	v_add3_u32 v9, s30, v84, v9
	v_or_b32_e32 v14, v9, v8
	v_cmp_gt_u32_e64 s[8:9], s8, v14
	s_and_saveexec_b64 s[6:7], s[8:9]
	v_lshl_or_b32 v7, v8, 7, v9
	s_movk_i32 s10, 0x48
	v_mad_i32_i24 v6, v84, -9, v83
	v_mul_lo_u32 v7, v7, s10
	v_lshl_add_u32 v6, v6, 3, v7
	v_mov_b32_e32 v7, 0
	s_or_b64 exec, exec, s[6:7]
	v_lshl_add_u64 v[6:7], v[6:7], 1, s[22:23]
	global_load_dwordx4 v[42:45], v[6:7], off
	v_or_b32_e32 v86, 0x800, v0
	v_mul_u32_u24_e32 v6, 0x1c72, v86
	v_lshrrev_b32_e32 v14, 16, v6
	v_mul_u32_u24_e32 v6, 0xca5, v86
	s_load_dwordx8 s[12:19], s[0:1], 0x28
	s_load_dwordx2 s[20:21], s[0:1], 0x18
	v_lshrrev_b32_e32 v6, 19, v6
	v_mul_i32_i24_e32 v7, 0xffffffee, v6
	v_add_u32_e32 v15, s29, v6
	v_add3_u32 v16, s30, v14, v7
	v_or_b32_e32 v6, v16, v15
	s_movk_i32 s26, 0x80
	v_cmp_gt_u32_e64 s[10:11], s26, v6
	v_mov_b64_e32 v[6:7], 0
	v_mov_b64_e32 v[8:9], 0
	s_and_saveexec_b64 s[6:7], s[10:11]
	v_lshl_or_b32 v9, v15, 7, v16
	s_movk_i32 s24, 0x48
	v_mad_i32_i24 v8, v14, -9, v86
	v_mul_lo_u32 v9, v9, s24
	v_lshl_add_u32 v8, v8, 3, v9
	v_mov_b32_e32 v9, 0
	s_or_b64 exec, exec, s[6:7]
	v_lshl_add_u64 v[8:9], v[8:9], 1, s[22:23]
	global_load_dwordx4 v[46:49], v[8:9], off
	v_or_b32_e32 v87, 0xa00, v0
	v_min_u32_e32 v8, 0xb63, v87
	v_mul_u32_u24_e32 v14, 0xca5, v8
	s_load_dwordx2 s[24:25], s[0:1], 0x10
	s_load_dwordx2 s[64:65], s[0:1], 0x48
	v_mul_u32_u24_e32 v9, 0x1c72, v8
	v_lshrrev_b32_e32 v14, 19, v14
	v_lshrrev_b32_e32 v9, 16, v9
	v_mul_i32_i24_e32 v15, 0xffffffee, v14
	v_add_u32_e32 v14, s29, v14
	v_add3_u32 v15, s30, v9, v15
	v_or_b32_e32 v16, v15, v14
	v_and_b32_e32 v59, 15, v0
	v_cmp_gt_u32_e64 s[6:7], s26, v16
	s_and_saveexec_b64 s[26:27], s[6:7]
	v_lshl_or_b32 v7, v14, 7, v15
	s_movk_i32 s31, 0x48
	v_mad_i32_i24 v6, v9, -9, v8
	v_mul_lo_u32 v7, v7, s31
	v_lshl_add_u32 v6, v6, 3, v7
	v_mov_b32_e32 v7, 0
	s_or_b64 exec, exec, s[26:27]
	v_lshl_add_u64 v[6:7], v[6:7], 1, s[22:23]
	s_movk_i32 s22, 0xe39
	global_load_dwordx4 v[38:41], v[6:7], off
	v_mul_u32_u24_sdwa v6, v0, s22 dst_sel:DWORD dst_unused:UNUSED_PAD src0_sel:WORD_0 src1_sel:DWORD
	v_lshrrev_b32_e32 v75, 16, v6
	v_or_b32_e32 v14, 0x200, v0
	s_movk_i32 s22, 0xffee
	s_movk_i32 s23, 0x48
	v_mul_u32_u24_e32 v6, 0x48, v75
	v_mul_u32_u24_e32 v8, 0xe39, v14
	v_mad_i32_i24 v53, v75, s22, v0
	v_lshlrev_b32_e32 v50, 2, v6
	v_mov_b32_e32 v51, 0
	v_mul_i32_i24_sdwa v15, v8, s22 dst_sel:DWORD dst_unused:UNUSED_PAD src0_sel:WORD_1 src1_sel:DWORD
	v_mul_u32_u24_sdwa v8, v8, s23 dst_sel:DWORD dst_unused:UNUSED_PAD src0_sel:WORD_1 src1_sel:DWORD
	s_waitcnt lgkmcnt(0)
	v_lshl_add_u64 v[6:7], s[24:25], 0, v[50:51]
	v_lshlrev_b32_e32 v54, 2, v53
	v_lshlrev_b32_e32 v50, 2, v8
	v_add_lshl_u32 v14, v15, v14, 2
	v_ashrrev_i32_e32 v55, 31, v54
	v_lshl_add_u64 v[8:9], s[24:25], 0, v[50:51]
	v_ashrrev_i32_e32 v15, 31, v14
	v_lshl_add_u64 v[6:7], v[54:55], 2, v[6:7]
	v_lshl_add_u64 v[8:9], v[14:15], 2, v[8:9]
	global_load_dwordx4 v[18:21], v[6:7], off
	global_load_dwordx4 v[14:17], v[8:9], off
	v_min_u32_e32 v8, 0x50f, v61
	v_mul_u32_u24_e32 v6, 0xe39, v8
	v_mul_i32_i24_sdwa v9, v6, s22 dst_sel:DWORD dst_unused:UNUSED_PAD src0_sel:WORD_1 src1_sel:DWORD
	v_mul_u32_u24_sdwa v6, v6, s23 dst_sel:DWORD dst_unused:UNUSED_PAD src0_sel:WORD_1 src1_sel:DWORD
	v_lshlrev_b32_e32 v50, 2, v6
	v_lshl_add_u64 v[6:7], s[24:25], 0, v[50:51]
	v_min_u32_e32 v50, 0x47, v0
	v_add_lshl_u32 v8, v9, v8, 2
	v_lshlrev_b32_e32 v50, 2, v50
	v_add_u32_e32 v63, -8, v59
	v_ashrrev_i32_e32 v9, 31, v8
	global_load_dword v68, v50, s[20:21]
	v_min_u32_e32 v50, 6, v59
	v_med3_i32 v64, v63, 0, 2
	v_mul_u32_u24_e32 v52, 7, v52
	v_and_b32_e32 v72, 15, v62
	v_lshl_add_u64 v[6:7], v[8:9], 2, v[6:7]
	v_lshlrev_b32_e32 v55, 2, v50
	v_lshlrev_b32_e32 v65, 2, v64
	v_add_lshl_u32 v50, v52, v50, 2
	v_lshrrev_b32_e32 v52, 4, v62
	v_add_u32_e32 v71, -8, v72
	global_load_dwordx4 v[6:9], v[6:7], off
	v_med3_i32 v67, v71, 0, 2
	global_load_dword v55, v55, s[14:15]
	s_nop 0
	global_load_dword v64, v65, s[18:19]
	global_load_dword v70, v65, s[16:17]
	v_min_u32_e32 v65, 6, v72
	v_mul_u32_u24_e32 v52, 7, v52
	v_add_lshl_u32 v52, v52, v65, 2
	global_load_dword v66, v50, s[12:13]
	global_load_dword v65, v52, s[12:13]
	v_mad_u32_u24 v50, 64, 3, v67
	v_add_u32_e32 v50, 0xffffff40, v50
	v_lshl_add_u64 v[88:89], v[50:51], 2, s[16:17]
	v_min_u32_e32 v50, 0x47f, v61
	v_lshrrev_b32_e32 v52, 4, v50
	v_and_b32_e32 v50, 15, v50
	v_add_u32_e32 v69, -8, v50
	s_movk_i32 s14, 0xff40
	v_min_u32_e32 v67, 6, v50
	v_med3_i32 v50, v69, 0, 2
	v_mul_u32_u24_e32 v52, 3, v52
	v_add3_u32 v50, v52, v50, s14
	global_load_dword v74, v[88:89], off
	v_lshlrev_b32_e32 v67, 2, v67
	v_lshl_add_u64 v[88:89], v[50:51], 2, s[16:17]
	global_load_dword v67, v67, s[12:13] offset:1764
	s_movk_i32 s12, 0x144
	global_load_dword v73, v[88:89], off
	v_cmp_gt_u32_e64 s[12:13], s12, v0
	s_and_saveexec_b64 s[14:15], s[12:13]
	s_cbranch_execz .LBB2_14
	v_mul_i32_i24_e32 v50, 0x1c72, v53
	v_lshrrev_b32_e32 v52, 31, v50
	v_add_u16_sdwa v50, v50, v52 dst_sel:DWORD dst_unused:UNUSED_PAD src0_sel:WORD_1 src1_sel:DWORD
	v_bfe_i32 v50, v50, 0, 16
	v_mul_i32_i24_e32 v52, -9, v50
	v_mad_u32_u24 v50, v75, 20, v50
	v_mul_i32_i24_e32 v50, 0xa0, v50
	v_add_lshl_u32 v52, v52, v53, 4
	v_add3_u32 v88, v50, 0, v52
	v_mov_b32_e32 v50, v51
	v_mov_b32_e32 v52, v51
	v_mov_b32_e32 v53, v51
	ds_write_b128 v88, v[50:53] offset:2880
